# baseline (speedup 1.0000x reference)
_Z11main_kernelPKcPf:
	s_load_dwordx2 s[8:9], s[0:1], 0x0
	v_mov_b32_e32 v63, 0
	v_lshlrev_b32_e32 v62, 4, v0
	s_mov_b32 s6, 0x3e0000
	s_and_b32 s4, s2, 15
	s_waitcnt lgkmcnt(0)
	s_ashr_i32 s22, s2, 7
	s_lshl_b32 s23, s2, 1
	s_and_b32 s23, s23, 0xe0
	s_lshl_b32 s22, s22, 8
	s_or_b32 s22, s22, s23
	v_and_b32_e32 v74, 31, v0
	v_or_b32_e32 v74, s22, v74
	v_lshlrev_b32_e32 v74, 8, v74
	v_bfe_u32 v76, v0, 5, 1
	v_lshl_add_u32 v74, v76, 7, v74
	v_mov_b32_e32 v75, 0
	v_lshl_add_u64 v[74:75], s[8:9], 0, v[74:75]
	v_readfirstlane_b32 s24, v0
	global_load_dwordx4 v[142:145], v[74:75], off
	global_load_dwordx4 v[146:149], v[74:75], off offset:16
	global_load_dwordx4 v[158:161], v[74:75], off offset:32
	global_load_dwordx4 v[162:165], v[74:75], off offset:48
	global_load_dwordx4 v[166:169], v[74:75], off offset:64
	global_load_dwordx4 v[170:173], v[74:75], off offset:80
	global_load_dwordx4 v[174:177], v[74:75], off offset:96
	global_load_dwordx4 v[178:181], v[74:75], off offset:112
	s_lshr_b32 s24, s24, 6
	s_cmp_gt_u32 s24, 3
	s_cbranch_scc1 .Lm_noq
	s_lshl_b32 s25, s22, 7
	s_add_u32 s26, s8, s25
	s_addc_u32 s27, s9, 0
	s_add_u32 s26, s26, 0x40000
	s_addc_u32 s27, s27, 0
	global_load_dwordx4 v[70:73], v62, s[26:27]
	s_cmp_lg_u32 s24, 0
	s_cbranch_scc1 .Lm_noq
	s_add_u32 s28, s8, 0x3ec000
	s_addc_u32 s29, s9, 0
	global_load_dwordx4 v[66:69], v62, s[28:29]
.Lm_noq:
	v_lshl_add_u64 v[2:3], s[8:9], 0, v[62:63]
	v_add_co_u32_e32 v18, vcc, s6, v2
	s_mov_b32 s6, 0x3e2000
	s_nop 0
	v_addc_co_u32_e32 v19, vcc, 0, v3, vcc
	v_add_co_u32_e32 v4, vcc, s6, v2
	s_mov_b32 s6, 0x3e4000
	s_nop 0
	v_addc_co_u32_e32 v5, vcc, 0, v3, vcc
	v_add_co_u32_e32 v6, vcc, s6, v2
	s_mov_b32 s6, 0x3e6000
	s_nop 0
	v_addc_co_u32_e32 v7, vcc, 0, v3, vcc
	s_ashr_i32 s3, s2, 7
	global_load_dwordx4 v[38:41], v[4:5], off
	global_load_dwordx4 v[42:45], v[6:7], off
	v_add_co_u32_e32 v4, vcc, s6, v2
	s_mul_i32 s5, s3, 0x700
	s_mulk_i32 s4, 0x70
	v_addc_co_u32_e32 v5, vcc, 0, v3, vcc
	s_mov_b32 s6, 0x3e8000
	s_add_i32 s4, s5, s4
	v_add_co_u32_e32 v6, vcc, s6, v2
	s_mul_hi_i32 s5, s4, 0x280
	s_mulk_i32 s4, 0x280
	v_addc_co_u32_e32 v7, vcc, 0, v3, vcc
	s_mov_b32 s6, 0x3ea000
	v_lshrrev_b32_e32 v1, 6, v0
	v_and_b32_e32 v64, 63, v0
	v_add_co_u32_e32 v20, vcc, s6, v2
	s_add_u32 s4, s8, s4
	v_mul_u32_u24_e32 v2, 0x230, v1
	v_addc_co_u32_e32 v21, vcc, 0, v3, vcc
	s_addc_u32 s5, s9, s5
	v_add_lshl_u32 v2, v2, v64, 4
	v_mov_b32_e32 v3, v63
	v_lshl_add_u64 v[22:23], s[4:5], 0, v[2:3]
	s_mov_b64 s[4:5], 0x60000
	v_lshl_add_u64 v[36:37], v[22:23], 0, s[4:5]
	s_mov_b32 s4, 0x60000
	v_add_co_u32_e32 v24, vcc, s4, v22
	global_load_dwordx4 v[46:49], v[4:5], off
	global_load_dwordx4 v[50:53], v[6:7], off
	v_addc_co_u32_e32 v25, vcc, 0, v23, vcc
	global_load_dwordx4 v[54:57], v[20:21], off
	global_load_dwordx4 v[2:5], v[24:25], off
	global_load_dwordx4 v[6:9], v[36:37], off offset:1024
	global_load_dwordx4 v[10:13], v[36:37], off offset:2048
	global_load_dwordx4 v[58:61], v[18:19], off
	global_load_dwordx4 v[14:17], v[36:37], off offset:3072
	v_add_co_u32_e32 v34, vcc, 0x61000, v22
	s_movk_i32 s4, 0x230
	s_nop 0
	v_addc_co_u32_e32 v35, vcc, 0, v23, vcc
	global_load_dwordx4 v[18:21], v[34:35], off
	global_load_dwordx4 v[22:25], v[34:35], off offset:1024
	global_load_dwordx4 v[26:29], v[34:35], off offset:2048
	global_load_dwordx4 v[30:33], v[34:35], off offset:3072
	v_or_b32_e32 v34, 0x200, v64
	v_cmp_gt_u32_e64 s[4:5], s4, v34
	s_and_saveexec_b64 s[6:7], s[4:5]
	s_cbranch_execz .LBB1_2
	v_add_co_u32_e32 v34, vcc, 0x2000, v36
	s_nop 1
	v_addc_co_u32_e32 v35, vcc, 0, v37, vcc
	global_load_dwordx4 v[34:37], v[34:35], off
.LBB1_2:
	s_or_b64 exec, exec, s[6:7]
	v_cmp_gt_u32_e32 vcc, 32, v0
	s_waitcnt vmcnt(5)
	ds_write_b128 v62, v[58:61]
	ds_write_b128 v62, v[38:41] offset:8192
	ds_write_b128 v62, v[42:45] offset:16384
	ds_write_b128 v62, v[46:49] offset:24576
	ds_write_b128 v62, v[50:53] offset:32768
	ds_write_b128 v62, v[54:57] offset:40960
	s_and_saveexec_b64 s[6:7], vcc
	s_cbranch_execz .LBB1_4
	v_mov_b32_e32 v63, 0
	ds_write_b128 v62, v[66:69] offset:49152
.LBB1_4:
	s_or_b64 exec, exec, s[6:7]
	s_lshl_b32 s6, s2, 1
	s_and_b32 s12, s6, 0xe0
	s_movk_i32 s6, 0xff
	s_movk_i32 s10, 0x100
	v_cmp_lt_u32_e64 s[6:7], s6, v0
	v_cmp_gt_u32_e32 vcc, s10, v0
	s_and_saveexec_b64 s[10:11], vcc
	s_cbranch_execz .LBB1_6
	v_lshrrev_b32_e32 v44, 3, v0
	v_and_b32_e32 v42, 0x70, v62
	v_mov_b32_e32 v43, 0
	s_movk_i32 s13, 0x90
	v_mad_u32_u24 v42, v44, s13, v42
	ds_write_b128 v42, v[70:73] offset:49664

.LBB1_12:
	s_or_b64 exec, exec, s[4:5]
	s_lshl_b32 s3, s3, 8
	s_or_b32 s3, s3, s12
	v_or_b32_e32 v2, s3, v220
	v_ashrrev_i32_e32 v3, 31, v2
	v_lshlrev_b64 v[2:3], 8, v[2:3]
	v_lshl_add_u64 v[2:3], s[8:9], 0, v[2:3]
	v_lshlrev_b32_e32 v112, 1, v115
	v_mov_b32_e32 v113, 0
	v_lshl_add_u64 v[2:3], v[2:3], 0, v[112:113]
	s_waitcnt lgkmcnt(0)
	s_barrier
	ds_read_b128 v[150:153], v218
	ds_read_b128 v[154:157], v218 offset:1024
	v_add_u32_e32 v56, v35, v114
	ds_read_b128 v[36:39], v218 offset:8192
	ds_read_b128 v[40:43], v218 offset:9216
	ds_read_b128 v[2:5], v56 offset:54784
	ds_read_b128 v[6:9], v56 offset:54816
	ds_read_b128 v[10:13], v56 offset:54848
	ds_read_b128 v[14:17], v56 offset:54880
	ds_read_b128 v[44:47], v56 offset:54272
	ds_read_b128 v[48:51], v56 offset:54304
	ds_read_b128 v[18:21], v56 offset:54656
	ds_read_b128 v[22:25], v56 offset:54688
	ds_read_b128 v[26:29], v56 offset:54720
	ds_read_b128 v[30:33], v56 offset:54752
	s_movk_i32 s3, 0x3dfd
	v_mov_b32_e32 v221, 0xc807
	s_movk_i32 s20, 0x4480
	s_mov_b32 s21, 0xbc04
	v_add_u32_e32 v35, v35, v115
	s_mov_b32 s4, 0
	s_mov_b32 s18, s4
	s_mov_b32 s19, s4
	s_mov_b32 s5, s4
	s_mov_b32 s6, s4
	s_mov_b32 s7, s4
	s_mov_b32 s8, s4
	s_mov_b32 s9, s4
	s_mov_b32 s10, s4
	s_mov_b32 s11, s4
	s_mov_b32 s12, s4
	s_mov_b32 s13, s4
	s_mov_b32 s14, s4
	s_mov_b32 s15, s4
	s_mov_b32 s16, s4
	s_mov_b32 s17, s4
	s_waitcnt vmcnt(7) lgkmcnt(5)
	v_pk_add_f16 v44, v142, v44
	v_pk_add_f16 v45, v143, v45
	v_pk_add_f16 v46, v144, v46
	v_pk_add_f16 v47, v145, v47
	v_or_b32_e32 v53, 0x80008000, v46
	v_or_b32_e32 v52, 0x80008000, v47
	v_or_b32_e32 v54, 0x80008000, v45
	v_or_b32_e32 v55, 0x80008000, v44
	v_pk_fma_f16 v61, v55, s3, v221 op_sel_hi:[1,0,0]
	v_pk_fma_f16 v62, v54, s3, v221 op_sel_hi:[1,0,0]
	v_pk_fma_f16 v63, v53, s3, v221 op_sel_hi:[1,0,0]
	v_pk_fma_f16 v64, v52, s3, v221 op_sel_hi:[1,0,0]
	v_pk_max_f16 v44, v44, 0
	v_pk_max_f16 v45, v45, 0
	v_pk_max_f16 v46, v46, 0
	v_pk_max_f16 v47, v47, 0
	v_pk_fma_f16 v64, v64, v52, s20 op_sel_hi:[1,1,0]
	v_pk_fma_f16 v63, v63, v53, s20 op_sel_hi:[1,1,0]
	v_pk_fma_f16 v62, v62, v54, s20 op_sel_hi:[1,1,0]
	v_pk_fma_f16 v61, v61, v55, s20 op_sel_hi:[1,1,0]
	v_pk_fma_f16 v62, v62, v54, s21 op_sel_hi:[1,1,0]
	v_pk_fma_f16 v61, v61, v55, s21 op_sel_hi:[1,1,0]
	v_pk_fma_f16 v63, v63, v53, s21 op_sel_hi:[1,1,0]
	v_pk_fma_f16 v64, v64, v52, s21 op_sel_hi:[1,1,0]
	s_waitcnt vmcnt(6) lgkmcnt(4)
	v_pk_add_f16 v48, v146, v48
	v_exp_f16_e32 v68, v61
	v_exp_f16_e32 v69, v62
	v_exp_f16_e32 v70, v63
	v_exp_f16_e32 v71, v64
	v_exp_f16_sdwa v68, v61 dst_sel:WORD_1 dst_unused:UNUSED_PRESERVE src0_sel:WORD_1
	v_exp_f16_sdwa v69, v62 dst_sel:WORD_1 dst_unused:UNUSED_PRESERVE src0_sel:WORD_1
	v_exp_f16_sdwa v70, v63 dst_sel:WORD_1 dst_unused:UNUSED_PRESERVE src0_sel:WORD_1
	v_exp_f16_sdwa v71, v64 dst_sel:WORD_1 dst_unused:UNUSED_PRESERVE src0_sel:WORD_1
	v_pk_add_f16 v49, v147, v49
	v_pk_fma_f16 v47, v52, v71, v47
	v_pk_fma_f16 v46, v53, v70, v46
	v_pk_fma_f16 v45, v54, v69, v45
	v_pk_fma_f16 v44, v55, v68, v44
	v_pk_add_f16 v50, v148, v50
	v_pk_add_f16 v51, v149, v51
	s_waitcnt lgkmcnt(0)
	v_mfma_f32_32x32x16_f16 v[18:33], v[150:153], v[44:47], v[18:33]
	v_or_b32_e32 v57, 0x80008000, v51
	v_or_b32_e32 v58, 0x80008000, v50
	v_or_b32_e32 v59, 0x80008000, v49
	v_or_b32_e32 v60, 0x80008000, v48
	v_pk_fma_f16 v65, v60, s3, v221 op_sel_hi:[1,0,0]
	v_pk_fma_f16 v66, v59, s3, v221 op_sel_hi:[1,0,0]
	v_pk_fma_f16 v67, v58, s3, v221 op_sel_hi:[1,0,0]
	v_mfma_f32_32x32x16_f16 v[2:17], v[36:39], v[44:47], v[2:17]
	v_pk_fma_f16 v52, v57, s3, v221 op_sel_hi:[1,0,0]
	v_pk_fma_f16 v53, v67, v58, s20 op_sel_hi:[1,1,0]
	v_pk_fma_f16 v52, v52, v57, s20 op_sel_hi:[1,1,0]
	v_pk_fma_f16 v54, v66, v59, s20 op_sel_hi:[1,1,0]
	v_pk_fma_f16 v55, v65, v60, s20 op_sel_hi:[1,1,0]
	v_pk_max_f16 v48, v48, 0
	v_pk_max_f16 v49, v49, 0
	v_pk_max_f16 v50, v50, 0
	v_pk_max_f16 v51, v51, 0
	v_pk_fma_f16 v55, v55, v60, s21 op_sel_hi:[1,1,0]
	v_pk_fma_f16 v54, v54, v59, s21 op_sel_hi:[1,1,0]
	v_pk_fma_f16 v36, v53, v58, s21 op_sel_hi:[1,1,0]
	v_pk_fma_f16 v37, v52, v57, s21 op_sel_hi:[1,1,0]
	s_nop 0
	v_exp_f16_e32 v44, v55
	v_exp_f16_e32 v45, v54
	v_exp_f16_e32 v38, v36
	v_exp_f16_e32 v39, v37
	v_exp_f16_sdwa v44, v55 dst_sel:WORD_1 dst_unused:UNUSED_PRESERVE src0_sel:WORD_1
	v_exp_f16_sdwa v45, v54 dst_sel:WORD_1 dst_unused:UNUSED_PRESERVE src0_sel:WORD_1
	v_exp_f16_sdwa v38, v36 dst_sel:WORD_1 dst_unused:UNUSED_PRESERVE src0_sel:WORD_1
	v_exp_f16_sdwa v39, v37 dst_sel:WORD_1 dst_unused:UNUSED_PRESERVE src0_sel:WORD_1
	s_nop 0
	v_pk_fma_f16 v39, v57, v39, v51
	v_pk_fma_f16 v38, v58, v38, v50
	v_pk_fma_f16 v37, v59, v45, v49
	v_pk_fma_f16 v36, v60, v44, v48
	ds_read_b128 v[44:47], v56 offset:54336
	ds_read_b128 v[48:51], v218 offset:2048
	v_mfma_f32_32x32x16_f16 v[18:33], v[154:157], v[36:39], v[18:33]
	v_mfma_f32_32x32x16_f16 v[2:17], v[40:43], v[36:39], v[2:17]
	s_waitcnt vmcnt(5) lgkmcnt(1)
	v_pk_add_f16 v40, v158, v44
	v_pk_add_f16 v41, v159, v45
	v_pk_add_f16 v42, v160, v46
	v_pk_add_f16 v43, v161, v47
	v_or_b32_e32 v45, 0x80008000, v42
	v_or_b32_e32 v44, 0x80008000, v43
	v_or_b32_e32 v46, 0x80008000, v41
	v_or_b32_e32 v47, 0x80008000, v40
	v_pk_fma_f16 v52, v47, s3, v221 op_sel_hi:[1,0,0]
	v_pk_fma_f16 v53, v46, s3, v221 op_sel_hi:[1,0,0]
	v_pk_fma_f16 v54, v45, s3, v221 op_sel_hi:[1,0,0]
	v_pk_fma_f16 v55, v44, s3, v221 op_sel_hi:[1,0,0]
	ds_read_b128 v[36:39], v56 offset:54368
	v_pk_fma_f16 v55, v55, v44, s20 op_sel_hi:[1,1,0]
	v_pk_fma_f16 v54, v54, v45, s20 op_sel_hi:[1,1,0]
	v_pk_fma_f16 v53, v53, v46, s20 op_sel_hi:[1,1,0]
	v_pk_fma_f16 v52, v52, v47, s20 op_sel_hi:[1,1,0]
	v_pk_max_f16 v40, v40, 0
	v_pk_max_f16 v41, v41, 0
	v_pk_max_f16 v42, v42, 0
	v_pk_max_f16 v43, v43, 0
	v_pk_fma_f16 v52, v52, v47, s21 op_sel_hi:[1,1,0]
	v_pk_fma_f16 v53, v53, v46, s21 op_sel_hi:[1,1,0]
	v_pk_fma_f16 v54, v54, v45, s21 op_sel_hi:[1,1,0]
	v_pk_fma_f16 v55, v55, v44, s21 op_sel_hi:[1,1,0]
	s_nop 0
	v_exp_f16_e32 v57, v52
	v_exp_f16_e32 v58, v53
	v_exp_f16_e32 v59, v54
	v_exp_f16_e32 v60, v55
	v_exp_f16_sdwa v57, v52 dst_sel:WORD_1 dst_unused:UNUSED_PRESERVE src0_sel:WORD_1
	v_exp_f16_sdwa v58, v53 dst_sel:WORD_1 dst_unused:UNUSED_PRESERVE src0_sel:WORD_1
	v_exp_f16_sdwa v59, v54 dst_sel:WORD_1 dst_unused:UNUSED_PRESERVE src0_sel:WORD_1
	v_exp_f16_sdwa v60, v55 dst_sel:WORD_1 dst_unused:UNUSED_PRESERVE src0_sel:WORD_1
	s_nop 0
	v_pk_fma_f16 v43, v44, v60, v43
	v_pk_fma_f16 v42, v45, v59, v42
	v_pk_fma_f16 v41, v46, v58, v41
	v_pk_fma_f16 v40, v47, v57, v40
	ds_read_b128 v[44:47], v218 offset:3072
	s_waitcnt vmcnt(4) lgkmcnt(1)
	v_pk_add_f16 v36, v162, v36
	v_mfma_f32_32x32x16_f16 v[18:33], v[48:51], v[40:43], v[18:33]
	ds_read_b128 v[48:51], v218 offset:10240
	ds_read_b128 v[52:55], v218 offset:11264
	v_pk_add_f16 v37, v163, v37
	v_pk_add_f16 v38, v164, v38
	v_pk_add_f16 v39, v165, v39
	s_waitcnt lgkmcnt(1)
	v_mfma_f32_32x32x16_f16 v[2:17], v[48:51], v[40:43], v[2:17]
	v_or_b32_e32 v40, 0x80008000, v39
	v_or_b32_e32 v41, 0x80008000, v38
	v_or_b32_e32 v42, 0x80008000, v37
	v_or_b32_e32 v43, 0x80008000, v36
	v_pk_fma_f16 v48, v43, s3, v221 op_sel_hi:[1,0,0]
	v_pk_fma_f16 v49, v42, s3, v221 op_sel_hi:[1,0,0]
	v_pk_fma_f16 v50, v41, s3, v221 op_sel_hi:[1,0,0]
	v_pk_fma_f16 v51, v40, s3, v221 op_sel_hi:[1,0,0]
	v_pk_fma_f16 v50, v50, v41, s20 op_sel_hi:[1,1,0]
	v_pk_fma_f16 v51, v51, v40, s20 op_sel_hi:[1,1,0]
	v_pk_fma_f16 v49, v49, v42, s20 op_sel_hi:[1,1,0]
	v_pk_fma_f16 v48, v48, v43, s20 op_sel_hi:[1,1,0]
	v_pk_max_f16 v36, v36, 0
	v_pk_max_f16 v37, v37, 0
	v_pk_max_f16 v38, v38, 0
	v_pk_max_f16 v39, v39, 0
	v_pk_fma_f16 v48, v48, v43, s21 op_sel_hi:[1,1,0]
	v_pk_fma_f16 v49, v49, v42, s21 op_sel_hi:[1,1,0]
	v_pk_fma_f16 v50, v50, v41, s21 op_sel_hi:[1,1,0]
	v_pk_fma_f16 v51, v51, v40, s21 op_sel_hi:[1,1,0]
	s_nop 0
	v_exp_f16_e32 v57, v48
	v_exp_f16_e32 v58, v49
	v_exp_f16_e32 v59, v50
	v_exp_f16_e32 v60, v51
	v_exp_f16_sdwa v57, v48 dst_sel:WORD_1 dst_unused:UNUSED_PRESERVE src0_sel:WORD_1
	v_exp_f16_sdwa v58, v49 dst_sel:WORD_1 dst_unused:UNUSED_PRESERVE src0_sel:WORD_1
	v_exp_f16_sdwa v59, v50 dst_sel:WORD_1 dst_unused:UNUSED_PRESERVE src0_sel:WORD_1
	v_exp_f16_sdwa v60, v51 dst_sel:WORD_1 dst_unused:UNUSED_PRESERVE src0_sel:WORD_1
	s_nop 0
	v_pk_fma_f16 v39, v40, v60, v39
	v_pk_fma_f16 v38, v41, v59, v38
	v_pk_fma_f16 v37, v42, v58, v37
	v_pk_fma_f16 v36, v43, v57, v36
	s_nop 1
	v_mfma_f32_32x32x16_f16 v[18:33], v[44:47], v[36:39], v[18:33]
	ds_read_b128 v[40:43], v56 offset:54400
	ds_read_b128 v[44:47], v218 offset:4096
	s_waitcnt vmcnt(3) lgkmcnt(1)
	v_pk_add_f16 v40, v166, v40
	v_pk_add_f16 v41, v167, v41
	v_pk_add_f16 v42, v168, v42
	v_pk_add_f16 v43, v169, v43
	v_mfma_f32_32x32x16_f16 v[2:17], v[52:55], v[36:39], v[2:17]
	v_or_b32_e32 v48, 0x80008000, v43
	v_or_b32_e32 v49, 0x80008000, v42
	v_or_b32_e32 v50, 0x80008000, v41
	v_or_b32_e32 v51, 0x80008000, v40
	v_pk_fma_f16 v52, v51, s3, v221 op_sel_hi:[1,0,0]
	v_pk_fma_f16 v53, v50, s3, v221 op_sel_hi:[1,0,0]
	v_pk_fma_f16 v54, v49, s3, v221 op_sel_hi:[1,0,0]
	v_pk_fma_f16 v55, v48, s3, v221 op_sel_hi:[1,0,0]
	ds_read_b128 v[36:39], v56 offset:54432
	v_pk_fma_f16 v55, v55, v48, s20 op_sel_hi:[1,1,0]
	v_pk_fma_f16 v54, v54, v49, s20 op_sel_hi:[1,1,0]
	v_pk_fma_f16 v53, v53, v50, s20 op_sel_hi:[1,1,0]
	v_pk_fma_f16 v52, v52, v51, s20 op_sel_hi:[1,1,0]
	v_pk_max_f16 v40, v40, 0
	v_pk_max_f16 v41, v41, 0
	v_pk_max_f16 v42, v42, 0
	v_pk_max_f16 v43, v43, 0
	v_pk_fma_f16 v52, v52, v51, s21 op_sel_hi:[1,1,0]
	v_pk_fma_f16 v53, v53, v50, s21 op_sel_hi:[1,1,0]
	v_pk_fma_f16 v54, v54, v49, s21 op_sel_hi:[1,1,0]
	v_pk_fma_f16 v55, v55, v48, s21 op_sel_hi:[1,1,0]
	s_nop 0
	v_exp_f16_e32 v57, v52
	v_exp_f16_e32 v58, v53
	v_exp_f16_e32 v59, v54
	v_exp_f16_e32 v60, v55
	v_exp_f16_sdwa v57, v52 dst_sel:WORD_1 dst_unused:UNUSED_PRESERVE src0_sel:WORD_1
	v_exp_f16_sdwa v58, v53 dst_sel:WORD_1 dst_unused:UNUSED_PRESERVE src0_sel:WORD_1
	v_exp_f16_sdwa v59, v54 dst_sel:WORD_1 dst_unused:UNUSED_PRESERVE src0_sel:WORD_1
	v_exp_f16_sdwa v60, v55 dst_sel:WORD_1 dst_unused:UNUSED_PRESERVE src0_sel:WORD_1
	s_nop 0
	v_pk_fma_f16 v43, v48, v60, v43
	v_pk_fma_f16 v42, v49, v59, v42
	v_pk_fma_f16 v41, v50, v58, v41
	v_pk_fma_f16 v40, v51, v57, v40
	ds_read_b128 v[48:51], v218 offset:5120
	s_waitcnt vmcnt(2) lgkmcnt(1)
	v_pk_add_f16 v36, v170, v36
	v_mfma_f32_32x32x16_f16 v[18:33], v[44:47], v[40:43], v[18:33]
	ds_read_b128 v[44:47], v218 offset:12288
	ds_read_b128 v[52:55], v218 offset:13312
	v_pk_add_f16 v37, v171, v37
	v_pk_add_f16 v38, v172, v38
	v_pk_add_f16 v39, v173, v39
	s_waitcnt lgkmcnt(1)
	v_mfma_f32_32x32x16_f16 v[2:17], v[44:47], v[40:43], v[2:17]
	v_or_b32_e32 v40, 0x80008000, v39
	v_or_b32_e32 v41, 0x80008000, v38
	v_or_b32_e32 v42, 0x80008000, v37
	v_or_b32_e32 v43, 0x80008000, v36
	v_pk_fma_f16 v44, v43, s3, v221 op_sel_hi:[1,0,0]
	v_pk_fma_f16 v45, v42, s3, v221 op_sel_hi:[1,0,0]
	v_pk_fma_f16 v46, v41, s3, v221 op_sel_hi:[1,0,0]
	v_pk_fma_f16 v47, v40, s3, v221 op_sel_hi:[1,0,0]
	v_pk_fma_f16 v46, v46, v41, s20 op_sel_hi:[1,1,0]
	v_pk_fma_f16 v47, v47, v40, s20 op_sel_hi:[1,1,0]
	v_pk_fma_f16 v45, v45, v42, s20 op_sel_hi:[1,1,0]
	v_pk_fma_f16 v44, v44, v43, s20 op_sel_hi:[1,1,0]
	v_pk_fma_f16 v45, v45, v42, s21 op_sel_hi:[1,1,0]
	v_pk_fma_f16 v44, v44, v43, s21 op_sel_hi:[1,1,0]
	v_pk_fma_f16 v46, v46, v41, s21 op_sel_hi:[1,1,0]
	v_pk_fma_f16 v47, v47, v40, s21 op_sel_hi:[1,1,0]
	v_pk_max_f16 v36, v36, 0
	v_pk_max_f16 v37, v37, 0
	v_pk_max_f16 v38, v38, 0
	v_pk_max_f16 v39, v39, 0
	v_exp_f16_e32 v57, v44
	v_exp_f16_e32 v58, v45
	v_exp_f16_e32 v59, v46
	v_exp_f16_e32 v60, v47
	v_exp_f16_sdwa v57, v44 dst_sel:WORD_1 dst_unused:UNUSED_PRESERVE src0_sel:WORD_1
	v_exp_f16_sdwa v58, v45 dst_sel:WORD_1 dst_unused:UNUSED_PRESERVE src0_sel:WORD_1
	v_exp_f16_sdwa v59, v46 dst_sel:WORD_1 dst_unused:UNUSED_PRESERVE src0_sel:WORD_1
	v_exp_f16_sdwa v60, v47 dst_sel:WORD_1 dst_unused:UNUSED_PRESERVE src0_sel:WORD_1
	s_nop 0
	v_pk_fma_f16 v39, v40, v60, v39
	v_pk_fma_f16 v38, v41, v59, v38
	v_pk_fma_f16 v37, v42, v58, v37
	v_pk_fma_f16 v36, v43, v57, v36
	ds_read_b128 v[40:43], v56 offset:54464
	ds_read_b128 v[44:47], v218 offset:6144
	v_mfma_f32_32x32x16_f16 v[18:33], v[48:51], v[36:39], v[18:33]
	s_waitcnt vmcnt(1) lgkmcnt(1)
	v_pk_add_f16 v40, v174, v40
	v_pk_add_f16 v41, v175, v41
	v_pk_add_f16 v42, v176, v42
	v_pk_add_f16 v43, v177, v43
	v_or_b32_e32 v49, 0x80008000, v42
	v_mfma_f32_32x32x16_f16 v[2:17], v[52:55], v[36:39], v[2:17]
	v_or_b32_e32 v48, 0x80008000, v43
	v_or_b32_e32 v50, 0x80008000, v41
	v_or_b32_e32 v51, 0x80008000, v40
	v_pk_fma_f16 v52, v51, s3, v221 op_sel_hi:[1,0,0]
	v_pk_fma_f16 v53, v50, s3, v221 op_sel_hi:[1,0,0]
	v_pk_fma_f16 v54, v49, s3, v221 op_sel_hi:[1,0,0]
	v_pk_fma_f16 v55, v48, s3, v221 op_sel_hi:[1,0,0]
	ds_read_b128 v[36:39], v56 offset:54496
	v_pk_fma_f16 v55, v55, v48, s20 op_sel_hi:[1,1,0]
	v_pk_fma_f16 v54, v54, v49, s20 op_sel_hi:[1,1,0]
	v_pk_fma_f16 v53, v53, v50, s20 op_sel_hi:[1,1,0]
	v_pk_fma_f16 v52, v52, v51, s20 op_sel_hi:[1,1,0]
	v_pk_max_f16 v40, v40, 0
	v_pk_max_f16 v41, v41, 0
	v_pk_max_f16 v42, v42, 0
	v_pk_max_f16 v43, v43, 0
	v_pk_fma_f16 v52, v52, v51, s21 op_sel_hi:[1,1,0]
	v_pk_fma_f16 v53, v53, v50, s21 op_sel_hi:[1,1,0]
	v_pk_fma_f16 v54, v54, v49, s21 op_sel_hi:[1,1,0]
	v_pk_fma_f16 v55, v55, v48, s21 op_sel_hi:[1,1,0]
	s_waitcnt vmcnt(0) lgkmcnt(0)
	v_pk_add_f16 v36, v178, v36
	v_exp_f16_e32 v56, v52
	v_exp_f16_e32 v57, v53
	v_exp_f16_e32 v58, v54
	v_exp_f16_e32 v59, v55
	v_exp_f16_sdwa v56, v52 dst_sel:WORD_1 dst_unused:UNUSED_PRESERVE src0_sel:WORD_1
	v_exp_f16_sdwa v57, v53 dst_sel:WORD_1 dst_unused:UNUSED_PRESERVE src0_sel:WORD_1
	v_exp_f16_sdwa v58, v54 dst_sel:WORD_1 dst_unused:UNUSED_PRESERVE src0_sel:WORD_1
	v_exp_f16_sdwa v59, v55 dst_sel:WORD_1 dst_unused:UNUSED_PRESERVE src0_sel:WORD_1
	v_pk_add_f16 v37, v179, v37
	v_pk_fma_f16 v43, v48, v59, v43
	v_pk_fma_f16 v42, v49, v58, v42
	v_pk_fma_f16 v41, v50, v57, v41
	v_pk_fma_f16 v40, v51, v56, v40
	ds_read_b128 v[48:51], v218 offset:7168
	v_pk_add_f16 v38, v180, v38
	v_mfma_f32_32x32x16_f16 v[18:33], v[44:47], v[40:43], v[18:33]
	ds_read_b128 v[44:47], v218 offset:14336
	ds_read_b128 v[52:55], v218 offset:15360
	v_pk_add_f16 v39, v181, v39
	s_waitcnt lgkmcnt(1)
	v_mfma_f32_32x32x16_f16 v[2:17], v[44:47], v[40:43], v[2:17]
	v_or_b32_e32 v40, 0x80008000, v39
	v_or_b32_e32 v41, 0x80008000, v38
	v_or_b32_e32 v42, 0x80008000, v37
	v_or_b32_e32 v43, 0x80008000, v36
	v_pk_fma_f16 v44, v43, s3, v221 op_sel_hi:[1,0,0]
	v_pk_fma_f16 v45, v42, s3, v221 op_sel_hi:[1,0,0]
	v_pk_fma_f16 v46, v41, s3, v221 op_sel_hi:[1,0,0]
	v_pk_fma_f16 v47, v40, s3, v221 op_sel_hi:[1,0,0]
	v_pk_fma_f16 v46, v46, v41, s20 op_sel_hi:[1,1,0]
	v_pk_fma_f16 v47, v47, v40, s20 op_sel_hi:[1,1,0]
	v_pk_fma_f16 v45, v45, v42, s20 op_sel_hi:[1,1,0]
	v_pk_fma_f16 v44, v44, v43, s20 op_sel_hi:[1,1,0]
	v_pk_max_f16 v36, v36, 0
	v_pk_max_f16 v37, v37, 0
	v_pk_max_f16 v38, v38, 0
	v_pk_max_f16 v39, v39, 0
	v_pk_fma_f16 v44, v44, v43, s21 op_sel_hi:[1,1,0]
	v_pk_fma_f16 v45, v45, v42, s21 op_sel_hi:[1,1,0]
	v_pk_fma_f16 v46, v46, v41, s21 op_sel_hi:[1,1,0]
	v_pk_fma_f16 v47, v47, v40, s21 op_sel_hi:[1,1,0]
	s_nop 0
	v_exp_f16_e32 v56, v44
	v_exp_f16_e32 v57, v45
	v_exp_f16_e32 v58, v46
	v_exp_f16_e32 v59, v47
	v_exp_f16_sdwa v56, v44 dst_sel:WORD_1 dst_unused:UNUSED_PRESERVE src0_sel:WORD_1
	v_exp_f16_sdwa v57, v45 dst_sel:WORD_1 dst_unused:UNUSED_PRESERVE src0_sel:WORD_1
	v_exp_f16_sdwa v58, v46 dst_sel:WORD_1 dst_unused:UNUSED_PRESERVE src0_sel:WORD_1
	v_exp_f16_sdwa v59, v47 dst_sel:WORD_1 dst_unused:UNUSED_PRESERVE src0_sel:WORD_1
	s_nop 0
	v_pk_fma_f16 v39, v40, v59, v39
	v_pk_fma_f16 v38, v41, v58, v38
	v_pk_fma_f16 v37, v42, v57, v37
	v_pk_fma_f16 v36, v43, v56, v36
	s_nop 1
	v_mfma_f32_32x32x16_f16 v[18:33], v[48:51], v[36:39], v[18:33]
	s_waitcnt lgkmcnt(0)
	v_mfma_f32_32x32x16_f16 v[2:17], v[52:55], v[36:39], v[2:17]
	ds_read_b128 v[48:51], v218 offset:16384
	ds_read_b128 v[52:55], v218 offset:17408
	ds_read_b128 v[36:39], v35 offset:54528
	s_nop 6
	v_cvt_pk_f16_f32 v122, v18, v19
	v_mov_b32_e32 v18, 0x1ec00
	v_cvt_pk_f16_f32 v116, v24, v25
	v_cvt_pk_f16_f32 v117, v22, v23
	v_cvt_pk_f16_f32 v120, v20, v21
	v_lshl_add_u32 v222, v34, 2, v18
	ds_read_b128 v[56:59], v35 offset:54544
	ds_read_b128 v[60:63], v35 offset:54560
	ds_read_b128 v[64:67], v35 offset:54576
	s_waitcnt lgkmcnt(3)
	v_pk_add_f16 v25, v39, v116
	v_pk_add_f16 v24, v38, v117
	v_pk_add_f16 v23, v37, v120
	v_pk_add_f16 v22, v36, v122
	v_cvt_pk_f16_f32 v112, v32, v33
	ds_read_b128 v[32:35], v222
	ds_read_b128 v[36:39], v222 offset:1024
	ds_read_b128 v[40:43], v222 offset:2048
	ds_read_b128 v[44:47], v222 offset:3072
	s_waitcnt lgkmcnt(0)
	v_mfma_f32_32x32x16_f16 v[32:47], v[48:51], v[22:25], v[32:47]
	v_cvt_pk_f16_f32 v128, v30, v31
	v_cvt_pk_f16_f32 v129, v28, v29
	v_cvt_pk_f16_f32 v130, v26, v27
	v_pk_add_f16 v21, v59, v112
	v_pk_add_f16 v20, v58, v128
	v_pk_add_f16 v19, v57, v129
	v_pk_add_f16 v18, v56, v130
	v_cvt_pk_f16_f32 v118, v8, v9
	v_cvt_pk_f16_f32 v121, v6, v7
	ds_read_b128 v[6:9], v218 offset:18432
	v_mfma_f32_32x32x16_f16 v[32:47], v[52:55], v[18:21], v[32:47]
	v_cvt_pk_f16_f32 v124, v4, v5
	v_cvt_pk_f16_f32 v126, v2, v3
	v_pk_add_f16 v29, v63, v118
	v_pk_add_f16 v28, v62, v121
	v_pk_add_f16 v27, v61, v124
	v_pk_add_f16 v26, v60, v126
	ds_read_b128 v[2:5], v218 offset:19456
	ds_read_b128 v[48:51], v218 offset:20480
	s_waitcnt lgkmcnt(2)
	v_mfma_f32_32x32x16_f16 v[32:47], v[6:9], v[26:29], v[32:47]
	v_cvt_pk_f16_f32 v119, v16, v17
	v_cvt_pk_f16_f32 v123, v14, v15
	v_cvt_pk_f16_f32 v125, v12, v13
	v_cvt_pk_f16_f32 v127, v10, v11
	v_pk_add_f16 v67, v67, v119
	v_pk_add_f16 v66, v66, v123
	v_pk_add_f16 v65, v65, v125
	v_pk_add_f16 v64, v64, v127
	s_waitcnt lgkmcnt(1)
	s_nop 0
	v_mfma_f32_32x32x16_f16 v[32:47], v[2:5], v[64:67], v[32:47]
	ds_read_b128 v[2:5], v222 offset:4096
	ds_read_b128 v[6:9], v222 offset:5120
	ds_read_b128 v[10:13], v222 offset:6144
	ds_read_b128 v[14:17], v222 offset:7168
	ds_read_b128 v[52:55], v218 offset:21504
	s_nop 6
	v_cvt_pk_f16_f32 v30, v38, v39
	s_waitcnt lgkmcnt(1)
	v_mfma_f32_32x32x16_f16 v[2:17], v[48:51], v[22:25], v[2:17]
	v_pk_max_f16 v99, v30, 0
	v_cvt_pk_f16_f32 v30, v36, v37
	v_pk_max_f16 v98, v30, 0
	v_cvt_pk_f16_f32 v30, v34, v35
	v_pk_max_f16 v97, v30, 0
	v_cvt_pk_f16_f32 v30, v32, v33
	v_pk_max_f16 v96, v30, 0
	s_waitcnt lgkmcnt(0)
	v_mfma_f32_32x32x16_f16 v[2:17], v[52:55], v[18:21], v[2:17]
	ds_read_b128 v[48:51], v218 offset:22528
	ds_read_b128 v[52:55], v218 offset:23552
	ds_read_b128 v[68:71], v218 offset:24576
	v_cvt_pk_f16_f32 v38, v46, v47
	v_pk_max_f16 v103, v38, 0
	s_waitcnt lgkmcnt(2)
	v_mfma_f32_32x32x16_f16 v[2:17], v[48:51], v[26:29], v[2:17]
	s_waitcnt lgkmcnt(1)
	v_mfma_f32_32x32x16_f16 v[2:17], v[52:55], v[64:67], v[2:17]
	ds_read_b128 v[48:51], v222 offset:8192
	ds_read_b128 v[52:55], v222 offset:9216
	ds_read_b128 v[56:59], v222 offset:10240
	ds_read_b128 v[60:63], v222 offset:11264
	ds_read_b128 v[72:75], v218 offset:25600
	ds_read_b128 v[34:37], v218 offset:28672
	s_nop 5
	v_cvt_pk_f16_f32 v8, v8, v9
	s_waitcnt lgkmcnt(2)
	v_mfma_f32_32x32x16_f16 v[48:63], v[68:71], v[22:25], v[48:63]
	ds_read_b128 v[68:71], v218 offset:26624
	v_cvt_pk_f16_f32 v6, v6, v7
	v_pk_max_f16 v107, v8, 0
	v_pk_max_f16 v106, v6, 0
	v_cvt_pk_f16_f32 v8, v4, v5
	v_cvt_pk_f16_f32 v2, v2, v3
	v_pk_max_f16 v104, v2, 0
	s_waitcnt lgkmcnt(2)
	v_mfma_f32_32x32x16_f16 v[48:63], v[72:75], v[18:21], v[48:63]
	ds_read_b128 v[72:75], v218 offset:27648
	ds_read_b128 v[80:83], v222 offset:12288
	ds_read_b128 v[84:87], v222 offset:13312
	ds_read_b128 v[88:91], v222 offset:14336
	ds_read_b128 v[92:95], v222 offset:15360
	ds_read_b128 v[30:33], v218 offset:29696
	ds_read_b128 v[4:7], v218 offset:31744
	v_cvt_pk_f16_f32 v2, v16, v17
	v_pk_max_f16 v111, v2, 0
	v_cvt_pk_f16_f32 v2, v14, v15
	s_waitcnt lgkmcnt(2)
	v_mfma_f32_32x32x16_f16 v[80:95], v[34:37], v[22:25], v[80:95]
	v_cvt_pk_f16_f32 v22, v44, v45
	v_pk_max_f16 v102, v22, 0
	v_cvt_pk_f16_f32 v22, v42, v43
	v_pk_max_f16 v101, v22, 0
	ds_read_b128 v[22:25], v218 offset:30720
	v_pk_max_f16 v105, v8, 0
	v_pk_max_f16 v110, v2, 0
	s_waitcnt lgkmcnt(2)
	v_mfma_f32_32x32x16_f16 v[80:95], v[30:33], v[18:21], v[80:95]
	v_cvt_pk_f16_f32 v34, v40, v41
	v_pk_max_f16 v100, v34, 0
	s_waitcnt lgkmcnt(0)
	v_mfma_f32_32x32x16_f16 v[80:95], v[22:25], v[26:29], v[80:95]
	v_mfma_f32_32x32x16_f16 v[48:63], v[68:71], v[26:29], v[48:63]
	v_mfma_f32_32x32x16_f16 v[80:95], v[4:7], v[64:67], v[80:95]
	ds_read_b128 v[2:5], v218 offset:33792
	ds_read_b128 v[6:9], v218 offset:34816
	ds_read_b128 v[14:17], v218 offset:32768
	v_mfma_f32_32x32x16_f16 v[48:63], v[72:75], v[64:67], v[48:63]
	v_mov_b64_e32 v[78:79], s[18:19]
	v_mov_b64_e32 v[76:77], s[16:17]
	v_mov_b64_e32 v[74:75], s[14:15]
	v_mov_b64_e32 v[72:73], s[12:13]
	v_mov_b64_e32 v[70:71], s[10:11]
	v_mov_b64_e32 v[68:69], s[8:9]
	v_mov_b64_e32 v[66:67], s[6:7]
	v_mov_b64_e32 v[64:65], s[4:5]
	s_waitcnt lgkmcnt(0)
	s_nop 1
	v_mfma_f32_32x32x16_f16 v[18:33], v[14:17], v[96:99], v[64:79]
	s_nop 1
	s_mov_b32 s5, 0xd680
	v_mfma_f32_32x32x16_f16 v[18:33], v[2:5], v[100:103], v[18:33]
	v_cvt_pk_f16_f32 v2, v12, v13
	v_pk_max_f16 v109, v2, 0
	v_cvt_pk_f16_f32 v2, v10, v11
	v_pk_max_f16 v108, v2, 0
	v_cvt_pk_f16_f32 v2, v54, v55
	v_pk_max_f16 v55, v2, 0
	ds_read_b128 v[2:5], v218 offset:35840
	v_mfma_f32_32x32x16_f16 v[18:33], v[6:9], v[104:107], v[18:33]
	v_cvt_pk_f16_f32 v6, v52, v53
	v_pk_max_f16 v54, v6, 0
	v_cvt_pk_f16_f32 v6, v50, v51
	v_pk_max_f16 v53, v6, 0
	v_cvt_pk_f16_f32 v6, v48, v49
	v_pk_max_f16 v52, v6, 0
	ds_read_b128 v[6:9], v218 offset:36864
	s_waitcnt lgkmcnt(1)
	v_mfma_f32_32x32x16_f16 v[18:33], v[2:5], v[108:111], v[18:33]
	v_cvt_pk_f16_f32 v2, v62, v63
	v_pk_max_f16 v63, v2, 0
	v_cvt_pk_f16_f32 v2, v60, v61
	v_pk_max_f16 v62, v2, 0
	v_cvt_pk_f16_f32 v2, v58, v59
	v_pk_max_f16 v61, v2, 0
	ds_read_b128 v[2:5], v218 offset:37888
	s_waitcnt lgkmcnt(1)
	v_mfma_f32_32x32x16_f16 v[18:33], v[6:9], v[52:55], v[18:33]
	v_cvt_pk_f16_f32 v6, v56, v57
	v_pk_max_f16 v60, v6, 0
	v_cvt_pk_f16_f32 v6, v86, v87
	v_pk_max_f16 v59, v6, 0
	v_cvt_pk_f16_f32 v6, v84, v85
	v_pk_max_f16 v58, v6, 0
	ds_read_b128 v[6:9], v218 offset:38912
	s_waitcnt lgkmcnt(1)
	v_mfma_f32_32x32x16_f16 v[18:33], v[2:5], v[60:63], v[18:33]
	v_cvt_pk_f16_f32 v2, v82, v83
	v_pk_max_f16 v57, v2, 0
	v_cvt_pk_f16_f32 v2, v80, v81
	v_pk_max_f16 v56, v2, 0
	v_cvt_pk_f16_f32 v2, v94, v95
	v_pk_max_f16 v83, v2, 0
	ds_read_b128 v[2:5], v218 offset:39936
	s_waitcnt lgkmcnt(1)
	v_mfma_f32_32x32x16_f16 v[18:33], v[6:9], v[56:59], v[18:33]
	v_cvt_pk_f16_f32 v6, v92, v93
	v_pk_max_f16 v82, v6, 0
	v_cvt_pk_f16_f32 v6, v90, v91
	v_pk_max_f16 v81, v6, 0
	v_cvt_pk_f16_f32 v6, v88, v89
	v_pk_max_f16 v80, v6, 0
	ds_read_b128 v[6:9], v218 offset:41984
	s_waitcnt lgkmcnt(1)
	v_mfma_f32_32x32x16_f16 v[18:33], v[2:5], v[80:83], v[18:33]
	ds_read_b128 v[2:5], v218 offset:40960
	s_nop 10
	v_xor_b32_e32 v17, 0x80000000, v33
	v_xor_b32_e32 v16, 0x80000000, v32
	v_xor_b32_e32 v15, 0x80000000, v31
	v_xor_b32_e32 v14, 0x80000000, v30
	ds_read_b128 v[30:33], v218 offset:43008
	s_waitcnt lgkmcnt(1)
	s_nop 1
	v_mfma_f32_32x32x16_f16 v[34:49], v[2:5], v[96:99], v[64:79]
	s_nop 1
	v_xor_b32_e32 v11, 0x80000000, v27
	v_mfma_f32_32x32x16_f16 v[34:49], v[6:9], v[100:103], v[34:49]
	v_xor_b32_e32 v10, 0x80000000, v26
	v_xor_b32_e32 v9, 0x80000000, v25
	v_xor_b32_e32 v8, 0x80000000, v24
	ds_read_b128 v[24:27], v218 offset:44032
	v_xor_b32_e32 v5, 0x80000000, v21
	v_xor_b32_e32 v4, 0x80000000, v20
	v_xor_b32_e32 v3, 0x80000000, v19
	s_waitcnt lgkmcnt(1)
	v_mfma_f32_32x32x16_f16 v[34:49], v[30:33], v[104:107], v[34:49]
	v_xor_b32_e32 v2, 0x80000000, v18
	ds_read_b128 v[18:21], v218 offset:45056
	v_xor_b32_e32 v7, 0x80000000, v23
	v_xor_b32_e32 v6, 0x80000000, v22
	v_exp_f32 v64, v113
	v_exp_f32 v65, v113
	v_exp_f32 v66, v113
	v_exp_f32 v67, v113
	v_exp_f32 v68, v113
	v_exp_f32 v69, v113
	v_exp_f32 v70, v113
	v_exp_f32 v71, v113
	v_exp_f32 v72, v113
	v_exp_f32 v73, v113
	v_exp_f32 v74, v113
	v_exp_f32 v75, v113
	v_exp_f32 v76, v113
	v_exp_f32 v77, v113
	v_exp_f32 v78, v113
	v_exp_f32 v79, v113
	v_xor_b32_e32 v13, 0x80000000, v29
	v_pk_add_f32 v[32:33], v[78:79], 0 op_sel_hi:[1,0]
	s_waitcnt lgkmcnt(1)
	v_mfma_f32_32x32x16_f16 v[34:49], v[24:27], v[108:111], v[34:49]
	ds_read_b128 v[22:25], v218 offset:46080
	v_xor_b32_e32 v12, 0x80000000, v28
	v_fma_mix_f32 v216, v64, v122, v113 op_sel:[0,0,0] op_sel_hi:[0,1,0]
	v_fma_mix_f32 v217, v65, v122, v113 op_sel:[0,1,0] op_sel_hi:[0,1,0]
	v_add_f32_e64 v30, v76, 0
	v_add_f32_e64 v31, v77, 0
	v_add_f32_e64 v28, v74, 0
	v_add_f32_e64 v29, v75, 0
	v_pk_add_f32 v[26:27], v[72:73], 0 op_sel_hi:[1,0]
	s_waitcnt lgkmcnt(1)
	v_mfma_f32_32x32x16_f16 v[34:49], v[18:21], v[52:55], v[34:49]
	ds_read_b128 v[18:21], v218 offset:47104
	ds_read_b128 v[50:53], v218 offset:48128
	v_fma_mix_f32 v206, v64, v126, v113 op_sel:[0,0,0] op_sel_hi:[0,1,0]
	v_fma_mix_f32 v207, v65, v126, v113 op_sel:[0,1,0] op_sel_hi:[0,1,0]
	v_fma_mix_f32 v214, v66, v120, v113 op_sel:[0,0,0] op_sel_hi:[0,1,0]
	v_fma_mix_f32 v215, v67, v120, v113 op_sel:[0,1,0] op_sel_hi:[0,1,0]
	v_fma_mix_f32 v212, v68, v117, v113 op_sel:[0,0,0] op_sel_hi:[0,1,0]
	s_waitcnt lgkmcnt(2)
	v_mfma_f32_32x32x16_f16 v[34:49], v[22:25], v[60:63], v[34:49]
	v_add_f32_e64 v24, v70, 0
	v_add_f32_e64 v25, v71, 0
	v_add_f32_e64 v22, v68, 0
	v_add_f32_e64 v23, v69, 0
	v_fma_mix_f32 v213, v69, v117, v113 op_sel:[0,1,0] op_sel_hi:[0,1,0]
	v_fma_mix_f32 v210, v70, v116, v113 op_sel:[0,0,0] op_sel_hi:[0,1,0]
	v_fma_mix_f32 v211, v71, v116, v113 op_sel:[0,1,0] op_sel_hi:[0,1,0]
	v_fma_mix_f32 v208, v72, v130, v113 op_sel:[0,0,0] op_sel_hi:[0,1,0]
	v_fma_mix_f32 v209, v73, v130, v113 op_sel:[0,1,0] op_sel_hi:[0,1,0]
	s_waitcnt lgkmcnt(1)
	v_mfma_f32_32x32x16_f16 v[34:49], v[18:21], v[56:59], v[34:49]
	v_add_f32_e64 v20, v66, 0
	v_add_f32_e64 v21, v67, 0
	v_add_f32_e64 v18, v64, 0
	v_add_f32_e64 v19, v65, 0
	v_fma_mix_f32 v204, v74, v129, v113 op_sel:[0,0,0] op_sel_hi:[0,1,0]
	v_fma_mix_f32 v205, v75, v129, v113 op_sel:[0,1,0] op_sel_hi:[0,1,0]
	v_fma_mix_f32 v202, v76, v128, v113 op_sel:[0,0,0] op_sel_hi:[0,1,0]
	v_fma_mix_f32 v203, v77, v128, v113 op_sel:[0,1,0] op_sel_hi:[0,1,0]
	v_fma_mix_f32 v196, v78, v112, v113 op_sel:[0,0,0] op_sel_hi:[0,1,0]
	s_waitcnt lgkmcnt(0)
	v_mfma_f32_32x32x16_f16 v[34:49], v[50:53], v[80:83], v[34:49]
	v_mul_u32_u24_e32 v50, 14, v1
	v_mul_u32_u24_e32 v50, 0x280, v50
	v_or_b32_e32 v51, v50, v115
	v_add_u32_e32 v223, 0xd780, v51
	v_add3_u32 v224, v50, v114, s5
	v_mov_b64_e32 v[64:65], v[32:33]
	s_mov_b32 s5, 0x42200000
	s_nop 4
	v_xor_b32_e32 v49, 0x80000000, v49
	v_xor_b32_e32 v48, 0x80000000, v48
	v_xor_b32_e32 v47, 0x80000000, v47
	v_xor_b32_e32 v46, 0x80000000, v46
	v_xor_b32_e32 v45, 0x80000000, v45
	v_xor_b32_e32 v44, 0x80000000, v44
	v_xor_b32_e32 v43, 0x80000000, v43
	v_xor_b32_e32 v42, 0x80000000, v42
	v_xor_b32_e32 v41, 0x80000000, v41
	v_xor_b32_e32 v40, 0x80000000, v40
	v_xor_b32_e32 v39, 0x80000000, v39
	v_xor_b32_e32 v38, 0x80000000, v38
	v_xor_b32_e32 v37, 0x80000000, v37
	v_xor_b32_e32 v36, 0x80000000, v36
	v_xor_b32_e32 v35, 0x80000000, v35
	v_xor_b32_e32 v34, 0x80000000, v34
	v_mov_b64_e32 v[62:63], v[30:31]
	v_mov_b64_e32 v[60:61], v[28:29]
	v_mov_b64_e32 v[58:59], v[26:27]
	v_mov_b64_e32 v[56:57], v[24:25]
	v_mov_b64_e32 v[54:55], v[22:23]
	v_mov_b64_e32 v[52:53], v[20:21]
	v_mov_b64_e32 v[50:51], v[18:19]
	v_fma_mix_f32 v197, v79, v112, v113 op_sel:[0,1,0] op_sel_hi:[0,1,0]
	v_fma_mix_f32 v200, v66, v124, v113 op_sel:[0,0,0] op_sel_hi:[0,1,0]
	v_fma_mix_f32 v201, v67, v124, v113 op_sel:[0,1,0] op_sel_hi:[0,1,0]
	v_fma_mix_f32 v198, v68, v121, v113 op_sel:[0,0,0] op_sel_hi:[0,1,0]
	v_fma_mix_f32 v199, v69, v121, v113 op_sel:[0,1,0] op_sel_hi:[0,1,0]
	v_fma_mix_f32 v194, v70, v118, v113 op_sel:[0,0,0] op_sel_hi:[0,1,0]
	v_fma_mix_f32 v195, v71, v118, v113 op_sel:[0,1,0] op_sel_hi:[0,1,0]
	v_fma_mix_f32 v192, v72, v127, v113 op_sel:[0,0,0] op_sel_hi:[0,1,0]
	v_fma_mix_f32 v193, v73, v127, v113 op_sel:[0,1,0] op_sel_hi:[0,1,0]
	v_fma_mix_f32 v190, v74, v125, v113 op_sel:[0,0,0] op_sel_hi:[0,1,0]
	v_fma_mix_f32 v191, v75, v125, v113 op_sel:[0,1,0] op_sel_hi:[0,1,0]
	v_fma_mix_f32 v188, v76, v123, v113 op_sel:[0,0,0] op_sel_hi:[0,1,0]
	v_fma_mix_f32 v189, v77, v123, v113 op_sel:[0,1,0] op_sel_hi:[0,1,0]
	v_fma_mix_f32 v186, v78, v119, v113 op_sel:[0,0,0] op_sel_hi:[0,1,0]
	v_fma_mix_f32 v187, v79, v119, v113 op_sel:[0,1,0] op_sel_hi:[0,1,0]
	s_branch .LBB1_14
